# baseline (speedup 1.0000x reference)
_Z11gemm_kernelILi128ELi192ELi1EEv8GemmArgs:
	s_load_dwordx2 s[4:5], s[0:1], 0x38
	s_addk_i32 s2, 0xe0
	s_mov_b32 s3, 0
	s_lshl_b64 s[6:7], s[2:3], 2
	s_waitcnt lgkmcnt(0)
	s_add_u32 s4, s4, s6
	s_addc_u32 s5, s5, s7
	s_load_dword s8, s[4:5], 0x0
	s_waitcnt lgkmcnt(0)
	s_cmp_lt_i32 s8, 0
	s_cbranch_scc1 .LBB3_4
	s_load_dwordx2 s[6:7], s[0:1], 0x48
	s_load_dwordx2 s[4:5], s[0:1], 0x0
	v_lshlrev_b32_e32 v64, 4, v0
	v_and_b32_e32 v1, 32, v0
	v_bitop3_b32 v1, v64, v1, 48 bitop3:0x6c
	s_and_b32 s2, s8, 0xffff
	v_bfe_u32 v4, v0, 2, 4
	v_lshrrev_b32_e32 v2, 1, v0
	v_lshrrev_b32_e32 v1, 1, v1
	v_lshrrev_b32_e32 v6, 3, v0
	v_and_or_b32 v1, v2, 32, v1
	v_add_u32_e32 v5, s2, v4
	v_and_b32_e32 v7, 48, v6
	s_movk_i32 s10, 0x70
	v_add_lshl_u32 v22, v5, v7, 12
	v_mov_b32_e32 v23, 0
	v_lshlrev_b32_e32 v44, 1, v1
	v_bitop3_b32 v1, v6, s10, 64 bitop3:0xc8
	s_waitcnt lgkmcnt(0)
	v_lshl_add_u64 v[2:3], s[4:5], 0, v[22:23]
	v_mov_b32_e32 v45, v23
	v_add_lshl_u32 v48, v5, v1, 12
	v_mov_b32_e32 v49, v23
	s_lshr_b32 s10, s8, 24
	s_bfe_u32 s9, s8, 0x80010
	v_lshl_add_u64 v[46:47], v[2:3], 0, v[44:45]
	v_lshl_add_u64 v[2:3], s[4:5], 0, v[48:49]
	s_mulk_i32 s10, 0x300
	v_lshl_add_u64 v[50:51], v[2:3], 0, v[44:45]
	s_mul_i32 s8, s9, 0xc0
	v_or_b32_e32 v2, s10, v4
	v_add_u32_e32 v4, s8, v2
	v_or_b32_e32 v2, v4, v7
	v_lshlrev_b32_e32 v52, 12, v2
	v_mov_b32_e32 v53, v23
	v_lshl_add_u64 v[2:3], s[6:7], 0, v[52:53]
	v_add_lshl_u32 v56, v4, v1, 12
	v_mov_b32_e32 v57, v23
	v_lshl_add_u64 v[54:55], v[2:3], 0, v[44:45]
	v_lshl_add_u64 v[2:3], s[6:7], 0, v[56:57]
	v_add_u32_e32 v60, 0x80000, v52
	v_mov_b32_e32 v61, v23
	v_lshl_add_u64 v[58:59], v[2:3], 0, v[44:45]
	v_lshl_add_u64 v[2:3], s[6:7], 0, v[60:61]
	v_lshl_add_u64 v[62:63], v[2:3], 0, v[44:45]
	v_readfirstlane_b32 s16, v0
	s_cmp_lt_u32 s16, 256
	s_cbranch_scc1 .Ldn_noprio
	s_setprio 1
.Ldn_noprio:
	s_load_dwordx2 s[0:1], s[0:1], 0x98
	s_lshr_b32 s16, s16, 6
	s_lshl_b32 s16, s16, 10
	v_bfe_u32 v1, v0, 6, 2
	v_lshrrev_b32_e32 v80, 2, v0
	s_add_u32 m0, s16, 0
	s_nop 0
	global_load_lds_dwordx4 v[46:47], off
	s_add_u32 m0, s16, 8192
	s_nop 0
	global_load_lds_dwordx4 v[50:51], off
	s_add_u32 m0, s16, 16384
	s_nop 0
	global_load_lds_dwordx4 v[54:55], off
	s_add_u32 m0, s16, 24576
	s_nop 0
	global_load_lds_dwordx4 v[58:59], off
	s_add_u32 m0, s16, 32768
	s_nop 0
	global_load_lds_dwordx4 v[62:63], off
	s_add_u32 m0, s16, 40832
	s_nop 0
	global_load_lds_dwordx4 v[46:47], off offset:128
	s_add_u32 m0, s16, 49024
	s_nop 0
	global_load_lds_dwordx4 v[50:51], off offset:128
	s_add_u32 m0, s16, 57216
	s_nop 0
	global_load_lds_dwordx4 v[54:55], off offset:128
	s_add_u32 m0, s16, 65408
	s_nop 0
	global_load_lds_dwordx4 v[58:59], off offset:128
	s_add_u32 m0, s16, 73600
	s_nop 0
	global_load_lds_dwordx4 v[62:63], off offset:128
	s_mov_b32 s17, 0
	s_mov_b32 s18, 0xa000
	s_mov_b32 s19, 0x14000
	v_lshlrev_b32_e32 v25, 6, v0
	v_lshlrev_b32_e32 v27, 2, v0
	v_and_b32_e32 v24, 48, v0
	v_and_b32_e32 v25, 0x3c0, v25
	v_and_b32_e32 v27, 32, v27
	v_or_b32_e32 v26, v25, v24
	v_bitop3_b32 v87, v25, v27, v24 bitop3:0x36
	v_or_b32_e32 v24, v44, v60
	v_mov_b32_e32 v25, v23
	v_lshl_add_u64 v[24:25], s[6:7], 0, v[24:25]
	s_mov_b64 s[10:11], 0x100
	v_lshl_add_u64 v[70:71], v[24:25], 0, s[10:11]
	v_or_b32_e32 v24, v56, v44
	v_mov_b32_e32 v25, v23
	v_lshl_add_u64 v[24:25], s[6:7], 0, v[24:25]
	v_lshl_add_u64 v[72:73], v[24:25], 0, s[10:11]
	v_or_b32_e32 v24, v52, v44
	v_mov_b32_e32 v25, v23
	v_lshl_add_u64 v[24:25], s[6:7], 0, v[24:25]
	v_lshl_add_u64 v[74:75], v[24:25], 0, s[10:11]
	v_or_b32_e32 v24, v48, v44
	v_mov_b32_e32 v25, v23
	v_lshl_add_u64 v[24:25], s[4:5], 0, v[24:25]
	v_or_b32_e32 v22, v22, v44
	v_and_b32_e32 v81, 64, v80
	v_mul_u32_u24_e32 v86, 0x1800, v1
	v_lshl_add_u64 v[76:77], v[24:25], 0, s[10:11]
	v_lshl_add_u64 v[24:25], s[4:5], 0, v[22:23]
	v_bitop3_b32 v82, v26, v86, v27 bitop3:0xde
	v_lshlrev_b32_e32 v88, 7, v81
	v_lshl_add_u64 v[78:79], v[24:25], 0, s[10:11]
	s_mov_b64 s[4:5], 0
	v_mov_b32_e32 v22, v23
	v_mov_b32_e32 v24, v23
	v_mov_b32_e32 v25, v23
	v_mov_b32_e32 v50, v23
	v_mov_b32_e32 v51, v23
	v_mov_b32_e32 v52, v23
	v_mov_b32_e32 v54, v23
	v_mov_b32_e32 v55, v23
	v_mov_b32_e32 v56, v23
	v_mov_b32_e32 v58, v23
	v_mov_b32_e32 v59, v23
	v_mov_b32_e32 v60, v23
	v_mov_b32_e32 v66, v23
	v_mov_b32_e32 v67, v23
	v_mov_b32_e32 v68, v23
	v_mov_b32_e32 v69, v23
	v_mov_b32_e32 v62, v23
	v_mov_b32_e32 v63, v23
	v_mov_b32_e32 v64, v23
	v_mov_b32_e32 v65, v23
	v_mov_b32_e32 v42, v23
	v_mov_b32_e32 v43, v23
	v_mov_b32_e32 v44, v23
	v_mov_b32_e32 v46, v23
	v_mov_b32_e32 v47, v23
	v_mov_b32_e32 v48, v23
	v_mov_b32_e32 v30, v23
	v_mov_b32_e32 v31, v23
	v_mov_b32_e32 v32, v23
	v_mov_b32_e32 v33, v23
	v_mov_b32_e32 v34, v23
	v_mov_b32_e32 v35, v23
	v_mov_b32_e32 v36, v23
	v_mov_b32_e32 v37, v23
	v_mov_b32_e32 v38, v23
	v_mov_b32_e32 v39, v23
	v_mov_b32_e32 v40, v23
	v_mov_b32_e32 v41, v23
	v_mov_b32_e32 v26, v23
	v_mov_b32_e32 v27, v23
	v_mov_b32_e32 v28, v23
	v_mov_b32_e32 v29, v23
	s_waitcnt vmcnt(5) lgkmcnt(0)
	s_barrier
	s_nop 0
	s_nop 0
